# v049 + NA tile loop: the 32 v_pk_mul_f32 accumulator rescales split into scalar v_mul_f32 pairs (bit-identical)
# baseline (speedup 1.0000x reference)
; template <bool NB, int R0, int R1>
; __device__ __forceinline__ void na_tile(const f32x16& S, float& m_run, float& l_run, f32x16& O0, f32x16& O1, bf16x8 (&pf)[2], const LAS float* tabp, int mk) {
;     ...
;     l_run = l_run * alpha + ps; m_run = m_new;
; #pragma unroll
;     for (int r = 0; r < 16; ++r) { O0[r] *= alpha; O1[r] *= alpha; }
; __device__ __forceinline__ void ph_na2(const int vc, const Params& p, LAS unsigned char* lds) {
;     ...
;             for (int db = 0; db < 2; ++db) {
;                 if (!nb || half == 0) { O[0][db] = __builtin_amdgcn_mfma_f32_32x32x16_bf16(vf[db][0], p0[0], O[0][db], 0, 0, 0); O[0][db] = __builtin_amdgcn_mfma_f32_32x32x16_bf16(vf[db][1], p0[1], O[0][db], 0, 0, 0); }
;                 else O[0][db] = __builtin_amdgcn_mfma_f32_32x32x16_bf16(vf[db][0], p0[0], O[0][db], 0, 0, 0);
.LBB0_373:
	s_nop 8
	v_mul_f32_e32 v82, v66, v204
	v_mul_f32_e32 v83, v67, v204
	v_mul_f32_e32 v80, v64, v204
	v_mul_f32_e32 v81, v65, v204
	v_mul_f32_e32 v78, v62, v204
	v_mul_f32_e32 v79, v63, v204
	v_mul_f32_e32 v76, v60, v204
	v_mul_f32_e32 v77, v61, v204
	v_mul_f32_e32 v74, v58, v204
	v_mul_f32_e32 v75, v59, v204
	v_mul_f32_e32 v72, v56, v204
	v_mul_f32_e32 v73, v57, v204
	v_mul_f32_e32 v70, v54, v204
	v_mul_f32_e32 v71, v55, v204
	v_mul_f32_e32 v68, v52, v204
	v_mul_f32_e32 v69, v53, v204
	s_cmp_lg_u32 s35, 0
	s_cselect_b64 s[4:5], -1, 0
	s_xor_b64 s[20:21], s[20:21], -1
	s_and_b64 s[4:5], s[20:21], s[4:5]
	s_mov_b64 s[22:23], -1
	s_and_b64 vcc, exec, s[4:5]
	s_cbranch_vccz .LBB0_375
	s_mov_b64 s[22:23], 0
	s_waitcnt vmcnt(11)
	v_mfma_f32_32x32x16_bf16 v[52:67], v[148:151], v[164:167], v[68:83]

; template <bool NB, int R0, int R1>
; __device__ __forceinline__ void na_tile(const f32x16& S, float& m_run, float& l_run, f32x16& O0, f32x16& O1, bf16x8 (&pf)[2], const LAS float* tabp, int mk) {
;     ...
;     l_run = l_run * alpha + ps; m_run = m_new;
; #pragma unroll
;     for (int r = 0; r < 16; ++r) { O0[r] *= alpha; O1[r] *= alpha; }
; __device__ __forceinline__ void ph_na2(const int vc, const Params& p, LAS unsigned char* lds) {
;     ...
;             for (int db = 0; db < 2; ++db) {
;                 if (!nb || half == 0) { O[0][db] = __builtin_amdgcn_mfma_f32_32x32x16_bf16(vf[db][0], p0[0], O[0][db], 0, 0, 0); O[0][db] = __builtin_amdgcn_mfma_f32_32x32x16_bf16(vf[db][1], p0[1], O[0][db], 0, 0, 0); }
;                 else O[0][db] = __builtin_amdgcn_mfma_f32_32x32x16_bf16(vf[db][0], p0[0], O[0][db], 0, 0, 0);
;                 if (!nb || half == 1) { O[1][db] = __builtin_amdgcn_mfma_f32_32x32x16_bf16(vf[db][0], p1[0], O[1][db], 0, 0, 0); O[1][db] = __builtin_amdgcn_mfma_f32_32x32x16_bf16(vf[db][1], p1[1], O[1][db], 0, 0, 0); }
;                 else O[1][db] = __builtin_amdgcn_mfma_f32_32x32x16_bf16(vf[db][1], p1[1], O[1][db], 0, 0, 0);
.LBB0_377:
	s_cmp_eq_u32 s35, 0
	s_cselect_b64 s[36:37], -1, 0
	s_and_b64 s[20:21], s[20:21], s[36:37]
	s_nop 1
	v_mul_f32_e32 v82, v34, v182
	v_mul_f32_e32 v83, v35, v182
	v_mul_f32_e32 v80, v32, v182
	v_mul_f32_e32 v81, v33, v182
	v_mul_f32_e32 v78, v30, v182
	v_mul_f32_e32 v79, v31, v182
	v_mul_f32_e32 v76, v28, v182
	v_mul_f32_e32 v77, v29, v182
	v_mul_f32_e32 v74, v26, v182
	v_mul_f32_e32 v75, v27, v182
	v_mul_f32_e32 v72, v24, v182
	v_mul_f32_e32 v73, v25, v182
	v_mul_f32_e32 v70, v22, v182
	v_mul_f32_e32 v71, v23, v182
	v_mul_f32_e32 v68, v20, v182
	v_mul_f32_e32 v69, v21, v182
	v_cvt_pk_bf16_f32 v180, v180, v181
	v_cvt_pk_bf16_f32 v181, v183, v184
	s_mov_b64 s[22:23], -1
	s_and_b64 vcc, exec, s[20:21]
	s_cbranch_vccz .LBB0_379
	s_mov_b64 s[22:23], 0
	s_waitcnt vmcnt(10)
	v_mfma_f32_32x32x16_bf16 v[20:35], v[140:143], v[178:181], v[68:83]

; template <bool NB, int R0, int R1>
; __device__ __forceinline__ void na_tile(const f32x16& S, float& m_run, float& l_run, f32x16& O0, f32x16& O1, bf16x8 (&pf)[2], const LAS float* tabp, int mk) {
;     ...
;     l_run = l_run * alpha + ps; m_run = m_new;
; #pragma unroll
;     for (int r = 0; r < 16; ++r) { O0[r] *= alpha; O1[r] *= alpha; }
; __device__ __forceinline__ void ph_na2(const int vc, const Params& p, LAS unsigned char* lds) {
;     ...
;             for (int db = 0; db < 2; ++db) {
;                 if (!nb || half == 0) { O[0][db] = __builtin_amdgcn_mfma_f32_32x32x16_bf16(vf[db][0], p0[0], O[0][db], 0, 0, 0); O[0][db] = __builtin_amdgcn_mfma_f32_32x32x16_bf16(vf[db][1], p0[1], O[0][db], 0, 0, 0); }
;                 else O[0][db] = __builtin_amdgcn_mfma_f32_32x32x16_bf16(vf[db][0], p0[0], O[0][db], 0, 0, 0);
;                 if (!nb || half == 1) { O[1][db] = __builtin_amdgcn_mfma_f32_32x32x16_bf16(vf[db][0], p1[0], O[1][db], 0, 0, 0); O[1][db] = __builtin_amdgcn_mfma_f32_32x32x16_bf16(vf[db][1], p1[1], O[1][db], 0, 0, 0); }
;                 else O[1][db] = __builtin_amdgcn_mfma_f32_32x32x16_bf16(vf[db][1], p1[1], O[1][db], 0, 0, 0);
.LBB0_381:
	v_mov_b32_e32 v205, v204
	s_nop 3
	v_mov_b32_e32 v68, v204
	v_mov_b32_e32 v69, v204
	v_mul_f32_e32 v82, v50, v68
	v_mul_f32_e32 v83, v51, v69
	v_mul_f32_e32 v80, v48, v68
	v_mul_f32_e32 v81, v49, v69
	v_mul_f32_e32 v78, v46, v68
	v_mul_f32_e32 v79, v47, v69
	v_mul_f32_e32 v76, v44, v68
	v_mul_f32_e32 v77, v45, v69
	v_mul_f32_e32 v74, v42, v68
	v_mul_f32_e32 v75, v43, v69
	v_mul_f32_e32 v72, v40, v68
	v_mul_f32_e32 v73, v41, v69
	v_mul_f32_e32 v70, v38, v68
	v_mul_f32_e32 v71, v39, v69
	v_mul_f32_e32 v68, v36, v204
	v_mul_f32_e32 v69, v37, v205
	s_andn2_b64 vcc, exec, s[4:5]
	s_mov_b64 s[4:5], -1
	s_cbranch_vccnz .LBB0_383
	s_waitcnt vmcnt(9)
	v_mfma_f32_32x32x16_bf16 v[36:51], v[120:123], v[164:167], v[68:83]
	s_mov_b64 s[4:5], 0

; template <bool NB, int R0, int R1>
; __device__ __forceinline__ void na_tile(const f32x16& S, float& m_run, float& l_run, f32x16& O0, f32x16& O1, bf16x8 (&pf)[2], const LAS float* tabp, int mk) {
;     ...
;     l_run = l_run * alpha + ps; m_run = m_new;
; #pragma unroll
;     for (int r = 0; r < 16; ++r) { O0[r] *= alpha; O1[r] *= alpha; }
; __device__ __forceinline__ void ph_na2(const int vc, const Params& p, LAS unsigned char* lds) {
;     ...
;             for (int db = 0; db < 2; ++db) {
;                 if (!nb || half == 0) { O[0][db] = __builtin_amdgcn_mfma_f32_32x32x16_bf16(vf[db][0], p0[0], O[0][db], 0, 0, 0); O[0][db] = __builtin_amdgcn_mfma_f32_32x32x16_bf16(vf[db][1], p0[1], O[0][db], 0, 0, 0); }
;                 else O[0][db] = __builtin_amdgcn_mfma_f32_32x32x16_bf16(vf[db][0], p0[0], O[0][db], 0, 0, 0);
;                 if (!nb || half == 1) { O[1][db] = __builtin_amdgcn_mfma_f32_32x32x16_bf16(vf[db][0], p1[0], O[1][db], 0, 0, 0); O[1][db] = __builtin_amdgcn_mfma_f32_32x32x16_bf16(vf[db][1], p1[1], O[1][db], 0, 0, 0); }
;                 else O[1][db] = __builtin_amdgcn_mfma_f32_32x32x16_bf16(vf[db][1], p1[1], O[1][db], 0, 0, 0);
.LBB0_385:
	v_mov_b32_e32 v183, v182
	s_nop 2
	v_mov_b32_e32 v68, v182
	v_mov_b32_e32 v69, v182
	v_mul_f32_e32 v82, v18, v68
	v_mul_f32_e32 v83, v19, v69
	v_mul_f32_e32 v80, v16, v68
	v_mul_f32_e32 v81, v17, v69
	v_mul_f32_e32 v78, v14, v68
	v_mul_f32_e32 v79, v15, v69
	v_mul_f32_e32 v76, v12, v68
	v_mul_f32_e32 v77, v13, v69
	v_mul_f32_e32 v74, v10, v68
	v_mul_f32_e32 v75, v11, v69
	v_mul_f32_e32 v72, v8, v68
	v_mul_f32_e32 v73, v9, v69
	v_mul_f32_e32 v70, v6, v68
	v_mul_f32_e32 v71, v7, v69
	v_mul_f32_e32 v68, v4, v182
	v_mul_f32_e32 v69, v5, v183
	s_andn2_b64 vcc, exec, s[20:21]
	s_mov_b64 s[4:5], -1
	s_cbranch_vccnz .LBB0_387
	s_waitcnt vmcnt(8)
	v_mfma_f32_32x32x16_bf16 v[4:19], v[116:119], v[178:181], v[68:83]
	s_mov_b64 s[4:5], 0
